# table-row and lru_combine index mappings reversed so the workers with five chunk items get the fewest rows/iterations
# speedup vs baseline: 1.0074x; 1.0074x over previous
; __device__ __forceinline__ void cvt_table_i4(const float* src, unsigned char* dst, float* scl, float scl_mul, int gw, int ngw, int lane) {
;     for (int row = gw; row < 16384; row += ngw) {
;         const f32x4* sp = (const f32x4*)(src + (size_t)row * 1024 + 16 * lane);
;         const f32x4 a0 = sp[0], a1 = sp[1], a2 = sp[2], a3 = sp[3];
; __global__ void __launch_bounds__(NWAVES * 64, 2) hybrid_fwd(Params P) {
;     ...
;                 const int w2 = (wk < 16 ? wk : wk - 2), N2 = NWK - 2;
;                 cvt_table_i4(P.peer_v, ws + WS_VB, (float*)(ws + WS_VSC), 1.0f / 16.0f, w2 * NWAVES + wave, N2 * NWAVES, lane);
.LBB0_1969:
	s_and_b32 s0, s2, 0x7ffffffe
	s_add_u32 s10, s24, 0x8100
	s_addc_u32 s11, s25, 0
	s_cmp_lg_u32 s0, 48
	s_mov_b64 s[0:1], -1
	s_cbranch_scc0 .LBB0_2050
	s_sub_i32 s0, s2, 34
	s_cmp_lt_i32 s2, 48
	v_readlane_b32 s6, v255, 10
	v_readlane_b32 s7, v255, 11
	s_cselect_b32 s14, s6, s0
	s_sub_i32 s12, s26, 34
	s_lshl_b32 s0, s14, 3
	v_readlane_b32 s6, v254, 56
	s_add_i32 s16, s6, s0
	s_lshl_b32 s18, s12, 3
	s_cmpk_lt_i32 s16, 0x4000
	s_cselect_b64 s[20:21], -1, 0
	s_cmpk_gt_i32 s16, 0x3fff
	v_lshlrev_b32_e32 v18, 3, v182
	v_mov_b32_e32 v19, 0
	v_readlane_b32 s7, v254, 57
	s_cbranch_scc1 .LBB0_1975
	s_ashr_i32 s17, s16, 31
	s_sub_i32 s98, 0x6ef, s16
	s_ashr_i32 s99, s98, 31
	s_lshl_b64 s[0:1], s[98:99], 2
	s_add_u32 s0, s24, s0
	s_addc_u32 s1, s25, s1
	s_add_u32 s6, s0, 0x1b60000
	s_addc_u32 s7, s1, 0
	s_ashr_i32 s19, s18, 31
	s_lshl_b64 s[42:43], s[18:19], 2
	s_lshl_b64 s[0:1], s[98:99], 9
	s_add_u32 s0, s24, s0
	s_addc_u32 s1, s25, s1
	v_lshl_add_u64 v[2:3], s[0:1], 0, v[18:19]
	s_mov_b64 s[0:1], 0xe400000
	v_lshl_add_u64 v[2:3], v[2:3], 0, s[0:1]
	s_lshl_b64 s[44:45], s[18:19], 9
	s_lshl_b64 s[0:1], s[98:99], 12
	s_add_u32 s0, s90, s0
	v_lshlrev_b32_e32 v4, 6, v182
	v_mov_b32_e32 v5, v19
	s_addc_u32 s1, s91, s1
	v_lshl_add_u64 v[4:5], s[0:1], 0, v[4:5]
	v_lshl_add_u64 v[4:5], v[4:5], 0, 32
	s_lshl_b64 s[46:47], s[18:19], 12
	s_mov_b32 s3, 0xf800000
	v_mov_b32_e32 v1, 0x260
	s_mov_b32 s13, 0xc0e00000
	v_mov_b32_e32 v6, 0x40e00000
	s_mov_b32 s15, s98
	s_branch .LBB0_1973

; __device__ __forceinline__ void cvt_table_i4(const float* src, unsigned char* dst, float* scl, float scl_mul, int gw, int ngw, int lane) {
;     for (int row = gw; row < 16384; row += ngw) {
;         const f32x4* sp = (const f32x4*)(src + (size_t)row * 1024 + 16 * lane);
;         const f32x4 a0 = sp[0], a1 = sp[1], a2 = sp[2], a3 = sp[3];
; __global__ void __launch_bounds__(NWAVES * 64, 2) hybrid_fwd(Params P) {
;     ...
;                 cvt_table_i4(P.peer_u, ws + WS_UB, (float*)(ws + WS_USC), 1.0f, w2 * NWAVES + wave, N2 * NWAVES, lane);
.LBB0_2022:
	s_or_b64 exec, exec, s[0:1]
	s_andn2_b64 vcc, exec, s[20:21]
	s_waitcnt vmcnt(0)
	s_barrier
	s_cbranch_vccnz .LBB0_2027
	s_sub_i32 s16, 0x6ef, s16
	s_ashr_i32 s17, s16, 31
	s_lshl_b64 s[0:1], s[16:17], 2
	s_add_u32 s0, s24, s0
	s_addc_u32 s1, s25, s1
	s_add_u32 s6, s0, 0x1b40000
	s_addc_u32 s7, s1, 0
	s_ashr_i32 s19, s18, 31
	s_lshl_b64 s[20:21], s[18:19], 2
	s_lshl_b64 s[0:1], s[16:17], 9
	s_add_u32 s0, s24, s0
	s_addc_u32 s1, s25, s1
	v_lshl_add_u64 v[2:3], s[0:1], 0, v[18:19]
	s_mov_b64 s[0:1], 0x6c00000
	v_lshl_add_u64 v[2:3], v[2:3], 0, s[0:1]
	s_lshl_b64 s[42:43], s[18:19], 9
	s_lshl_b64 s[0:1], s[16:17], 12
	s_add_u32 s0, s88, s0
	v_lshlrev_b32_e32 v4, 6, v182
	v_mov_b32_e32 v5, 0
	s_addc_u32 s1, s89, s1
	v_lshl_add_u64 v[6:7], s[0:1], 0, v[4:5]
	v_lshl_add_u64 v[6:7], v[6:7], 0, 32
	s_lshl_b64 s[44:45], s[18:19], 12
	s_mov_b32 s3, 0xf800000
	v_mov_b32_e32 v1, 0x260
	s_mov_b32 s13, 0xc0e00000
	v_mov_b32_e32 v4, 0x40e00000
	s_branch .LBB0_2025

; __device__ __forceinline__ void lru_combine(const Params& P, size_t wi, size_t nw) {
;     ...
;     for (size_t i = wi; i < (size_t)T * 64; i += nw) {
;         const size_t t = i >> 6; const int ch0 = (int)(i & 63) * 8;
;         const v4u hl = HLOC[i], pc = PCUM[i], gt = GATE[i];
; __global__ void __launch_bounds__(NWAVES * 64, 2) hybrid_fwd(Params P) {
;     ...
;                 lru_combine(P, (size_t)w2 * (NWAVES * 64) + tid, (size_t)N2 * (NWAVES * 64));
.LBB0_2046:
	s_or_b64 exec, exec, s[0:1]
	s_sub_i32 s14, 0xdd, s14
	s_lshl_b64 s[0:1], s[14:15], 9
	v_or_b32_e32 v2, s0, v0
	v_mov_b32_e32 v3, s1
	s_mov_b64 s[0:1], 0x100000
	v_cmp_gt_u64_e32 vcc, s[0:1], v[2:3]
	s_barrier
	s_and_saveexec_b64 s[6:7], vcc
	s_cbranch_execz .LBB0_2049
	s_ashr_i32 s13, s12, 31
	s_lshl_b64 s[16:17], s[12:13], 9
	s_add_u32 s18, s24, 0x280000
	s_addc_u32 s19, s25, 0
	s_lshl_b64 s[0:1], s[14:15], 13
	v_lshl_or_b32 v6, v0, 4, s0
	v_mov_b32_e32 v7, s1
	s_lshl_b64 s[0:1], s[14:15], 12
	v_mov_b32_e32 v5, 0
	s_lshl_b64 s[20:21], s[12:13], 13
	v_lshl_or_b32 v8, v0, 3, s0
	v_mov_b32_e32 v9, s1
	s_lshl_b64 s[12:13], s[12:13], 12
	s_mov_b64 s[14:15], 0
	s_mov_b32 s3, 0xffff0000
	s_movk_i32 s22, 0x7fff
	s_mov_b64 s[42:43], 0xfffff
